# conversion split: 26 tiles per conversion workgroup in P5 (2 more), P1 queue shortened by 256 tiles
# speedup vs baseline: 1.0026x; 1.0026x over previous
; #define LAS __attribute__((address_space(3)))
; #define SEAM(k) do { if (IN(k) && IN((k) + 1)) xcd_barrier(bar); } while (0)
; __device__ __forceinline__ void conv8_queue(const Ctx& X, int n) {
;     LAS int* qw = (LAS int*)(X.lds + LDS_MISC + 64);
;     unsigned zo = 0; asm volatile("" : "+v"(zo));
;     int nb_ = 0;
;     if (X.tid == 0) nb_ = (int)__hip_atomic_fetch_add(XP_ctl(X) + CW_WQ + zo, (unsigned)(8 * CQ_CHUNK), __ATOMIC_RELAXED, __HIP_MEMORY_SCOPE_AGENT);
; __global__ void __launch_bounds__(NTHR, 2) fwd(Args args) {
;     ...
;         conv8_queue(X, (X.G == 256) ? Q5_BASE : I_ALL8); } SEAM(1);
.LBB0_124:
	s_or_b64 exec, exec, s[8:9]
	s_mov_b32 s8, 0xe600
	s_and_b64 s[6:7], s[6:7], exec
	s_cselect_b32 s14, s8, 0x18000
	s_mov_b64 s[6:7], 0x14000
	s_add_u32 s15, s90, 0x50000000
	v_lshl_add_u64 v[68:69], v[2:3], 0, s[6:7]
	s_addc_u32 s16, s91, 0
	v_lshrrev_b32_e32 v2, 3, v194
	s_add_u32 s17, s90, 0x30000000
	v_lshl_or_b32 v77, s93, 5, v2
	v_lshlrev_b32_e32 v2, 4, v0
	s_addc_u32 s18, s91, 0
	v_and_b32_e32 v70, 0x70, v2
	v_lshlrev_b32_e32 v2, 2, v194
	s_movk_i32 s6, 0x90
	s_waitcnt lgkmcnt(0)
	s_add_i32 s20, 0, 0x23040
	v_mov_b32_e32 v71, v67
	s_lshl_b32 s19, s93, 4
	v_mul_u32_u24_e32 v78, 0x240, v194
	v_mul_lo_u32 v79, v77, s6
	s_mov_b32 s7, 0
	v_mov_b32_e32 v80, s20
	v_mov_b32_e32 v81, 16
	s_mov_b32 s21, 0xc3e00000
	v_lshlrev_b32_e32 v66, 2, v2
	v_mov_b32_e32 v82, 0x43e00000
	s_branch .LBB0_128

; __device__ __forceinline__ void conv8_fill(const Ctx& X, int base, int rank, int nblk, int n) { conv8b_run(X, (base >> 3) + rank, nblk, n); }
; #define SEAM(k) do { if (IN(k) && IN((k) + 1)) xcd_barrier(bar); } while (0)
; __device__ __forceinline__ Cvb conv8b_dec(const Ctx& X, int bit) { Cvb c; int kb, nb;
;     if (bit < I_GU8 / 8) { const int e = bit >> 8, r = bit & 255; kb = r >> 4; nb = r & 15; c.N = 2 * DFF; c.W = XP_w_gu(X) + (size_t)e * D * (2 * DFF); c.WT = XP_WguT(X) + (size_t)e * 16 * PAN_GU + (size_t)kb * PAN_GU; }
;     else { const int b2 = bit - I_GU8 / 8, e = b2 >> 7, r = b2 & 127; kb = r >> 3; nb = r & 7; c.N = D; c.W = XP_w_d(X) + (size_t)e * DFF * D; c.WT = XP_WdT(X) + (size_t)e * 16 * PAN_D + (size_t)kb * PAN_D; }
;     c.W += (size_t)(kb * 128 + 16 * X.wave) * c.N + nb * 256 + 4 * X.lane;
;     c.WT += (size_t)(nb * 256 + 32 * X.wave + (X.lane >> 3)) * 128 + 16 * (X.lane & 7);
;     return c; }
; __device__ __forceinline__ void conv8b_run(const Ctx& X, int first, int step, int count) {
;     if (count <= 0) return;
;     f32x4 v[16];
;     Cvb c = conv8b_dec(X, first), cn = c;
; #pragma unroll
;     for (int i = 0; i < 16; ++i) v[i] = __builtin_nontemporal_load((const f32x4*)(c.W + (size_t)i * c.N));
; __global__ void __launch_bounds__(NTHR, 2) fwd(Args args) {
;     ...
;     if (IN(5)) {
;         const int gb = (X.G == 256) ? P5_GEMM_BLOCKS : X.G;
;         if (X.bid < gb) { DenseSched S{(const char*)XP_MIX(X), (const char*)XP_WoutT(X), 64, T / 256, D / 256, (T / 256) * (D / 256), gb, X.bid}; EpiOut E{XP_x(X), XP_Hh(X)};
;             pg8::gemm_phase<EpiOut, DenseSched, false, false>(X.lds, D, 64, 64, (size_t)PANE_A * 2, (size_t)PANE_WOUT * 2, S, E); }
;         else conv8_fill(X, Q5_BASE, X.bid - gb, Q5_W / NWAVES, Q5_N); } SEAM(5);
.LBB0_721:
	s_cmp_lt_i32 s94, 6
	s_cselect_b64 s[4:5], -1, 0
	s_and_b64 s[2:3], s[4:5], s[2:3]
	s_andn2_b64 vcc, exec, s[2:3]
	s_cbranch_vccnz .LBB0_762
	s_cmpk_lg_i32 s92, 0x100
	s_cselect_b32 s30, s92, 0x80
	s_cmp_ge_i32 s87, s30
	s_mov_b64 s[4:5], -1
	s_cbranch_scc0 .LBB0_737
	s_load_dwordx2 s[6:7], s[0:1], 0x70
	s_load_dwordx2 s[8:9], s[0:1], 0x80
	s_sub_i32 s18, s87, s30
	s_lshl_b32 s18, s18, 1
	s_add_i32 s18, s18, 0x1cc0
	s_mov_b32 s19, 26
	s_mov_b32 s24, 0xc3e00000
	v_mov_b32_e32 v150, 0x43e00000
	v_lshlrev_b32_e32 v146, 4, v194
	v_mul_u32_u24_e32 v147, 0x240, v194
	s_lshl_b32 s20, s93, 4
	v_add_u32_e32 v147, s20, v147
	v_lshrrev_b32_e32 v151, 3, v194
	s_lshl_b32 s20, s93, 5
	v_add_u32_e32 v152, s20, v151
	v_mul_u32_u24_e32 v148, 0x90, v152
	v_and_b32_e32 v152, 7, v194
	v_lshl_add_u32 v148, v152, 4, v148
	v_lshlrev_b32_e32 v151, 7, v151
	v_lshl_add_u32 v149, v152, 4, v151
	s_waitcnt lgkmcnt(0)
	s_add_i32 s27, s18, 1
	s_cmp_lt_u32 s18, 0x2000
	s_cbranch_scc0 .Lcv5_dnP0
	s_lshr_b32 s20, s18, 4
	s_lshl_b32 s20, s20, 21
	s_and_b32 s21, s18, 15
	s_lshl_b32 s21, s21, 10
	s_add_u32 s20, s20, s21
	s_lshl_b32 s21, s93, 18
	s_add_u32 s20, s20, s21
	s_add_u32 s10, s6, s20
	s_addc_u32 s11, s7, 0
	s_movk_i32 s12, 0x4000
	s_lshl_b32 s20, s18, 15
	s_add_u32 s20, s20, 0x30000000
	s_branch .Lcv5_cmP0
